# cheap tail dummy loads in the conversion loop + the 128 mixer workgroups convert the last 256 tile pairs after their mixers
# speedup vs baseline: 1.0240x; 1.0000x over previous
; #define LAS __attribute__((address_space(3)))
; __device__ __forceinline__ int opaque_tid() { int t = threadIdx.x; asm volatile("" : "+v"(t)); return t; }
; #define REP(k) _Pragma("unroll") for (int rep_ = 0; rep_ < 1 + (int)(((REP_MASK) >> (k)) & 1u); ++rep_)
; __device__ __forceinline__ void ph_weights(const Params& p, LAS unsigned char* lds, const int p0, const int p1, const int wi, const int wn) {
;     const int tid = opaque_tid();
;     LAS unsigned* l32 = (LAS unsigned*)lds;
;     LAS bf16_t* l16 = (LAS bf16_t*)lds;
;     TDesc dA0, dA1, dB0, dB1; f32x4 a0[8], a1[8], b0[8], b1[8];
;     ...
;     int pi = p0 + wi; bool hA, hB;
;     PW_LOAD(pi, dA0, dA1, a0, a1, hA);
;     PW_LOAD(pi + wn, dB0, dB1, b0, b1, hB);
; __global__ void __launch_bounds__(512, 2) mk_fwd(Params p) {
;     ...
;         if (IN(pb + 2)) {
;             if (!split || bx < MIX_GW) {
;                 if (EN(5)) REP(5) ph_fft(p, lds, bx, vG);
;                 __syncthreads();
;                 if (EN(8)) REP(8) ph_mixers(p, l, lds, bx, vG);
;             } else { if (bx - MIX_GW < 4) ph_rbias(p, 0, bx - MIX_GW); ph_weights(p, lds, 240, 6880, bx - MIX_GW, G - MIX_GW); }
.LBB0_779:
	v_readlane_b32 s0, v249, 28
	s_nop 3
	s_add_u32 s0, s0, 80
	s_movk_i32 s70, 96
	s_movk_i32 s71, 0x1770
	s_mov_b32 s74, 0
	v_writelane_b32 v255, s29, 61
	s_branch .Lcv_common
.Lcv_late:
	v_readlane_b32 s0, v249, 28
	s_nop 3
	s_add_u32 s0, s0, 5872
	s_movk_i32 s70, 32
	s_movk_i32 s71, 0x19e0
	s_mov_b32 s74, 0
	v_writelane_b32 v255, s29, 61
	s_branch .Lcv_common
.Lcv_tail:
	v_writelane_b32 v246, s14, 0
	v_writelane_b32 v246, s15, 1
	v_writelane_b32 v246, s20, 2
	v_writelane_b32 v246, s21, 3
	v_writelane_b32 v246, s29, 4
	v_writelane_b32 v246, s30, 5
	v_writelane_b32 v246, s31, 6
	v_writelane_b32 v246, s36, 7
	v_writelane_b32 v246, s37, 8
	v_writelane_b32 v246, s56, 9
	v_writelane_b32 v246, s57, 10
	v_writelane_b32 v246, s69, 11
	s_mov_b32 s74, 2
	s_waitcnt vmcnt(0) lgkmcnt(0)
	s_barrier
	v_readlane_b32 s0, v249, 28
	s_nop 3
	s_add_u32 s0, s0, 6624
	s_movk_i32 s70, 128
	s_movk_i32 s71, 0x1ae0
.Lcv_common:
	s_lshl_b32 s72, s70, 1
	s_add_u32 s73, s72, s70
	s_waitcnt lgkmcnt(0)
	v_and_b32_e32 v166, 31, v0
	v_lshrrev_b32_e32 v167, 5, v0
	v_lshlrev_b32_e32 v168, 1, v167
	v_lshlrev_b32_e32 v169, 4, v166
	v_lshlrev_b32_e32 v170, 3, v167
	v_lshrrev_b32_e32 v1, 2, v167
	v_lshlrev_b32_e32 v1, 4, v1
	v_xor_b32_e32 v1, v169, v1
	v_lshl_add_u32 v154, v167, 9, v1
	v_xor_b32_e32 v155, 64, v154
	v_xor_b32_e32 v156, 0x80, v154
	v_xor_b32_e32 v157, 0xc0, v154
	v_and_b32_e32 v171, 15, v0
	v_lshrrev_b32_e32 v175, 4, v0
	v_lshlrev_b32_e32 v1, 2, v171
	v_xor_b32_e32 v1, v175, v1
	v_lshlrev_b32_e32 v174, 11, v171
	v_lshl_add_u32 v162, v1, 2, v174
	v_xor_b32_e32 v163, 0x80, v162
	v_xor_b32_e32 v164, 0x100, v162
	v_xor_b32_e32 v165, 0x180, v162
	v_lshlrev_b32_e32 v176, 4, v171
	v_add_u32_e32 v158, 0x10000, v154
	v_add_u32_e32 v159, 0x10000, v155
	v_add_u32_e32 v160, 0x10000, v156
	v_add_u32_e32 v161, 0x10000, v157
	v_add_u32_e32 v130, 0x10000, v162
	v_add_u32_e32 v131, 0x10000, v163
	v_add_u32_e32 v132, 0x10000, v164
	v_add_u32_e32 v133, 0x10000, v165
	s_mov_b32 s9, 3
	s_cmp_ge_u32 s0, 0xd70
	s_cselect_b32 s77, 1, 0
	s_mul_i32 s83, s77, 0xd70
	s_sub_u32 s78, s0, s83
	v_readlane_b32 s20, v249, 37
	v_readlane_b32 s21, v249, 38
	s_mov_b32 s29, 0
	s_cmpk_lt_u32 s78, 0xf0
	s_cbranch_scc1 .Lcv_win_A1
	s_cmpk_lt_u32 s78, 0x170
	s_cbranch_scc1 .Lcv_wout_A1
	s_cmpk_lt_u32 s78, 0x970
	s_cbranch_scc1 .Lcv_gu_A1
	s_sub_u32 s78, s78, 0x970
	s_lshr_b32 s83, s78, 6
	s_bfe_u32 s93, s78, 0x30003
	s_and_b32 s94, s78, 7
	s_mul_i32 s98, s77, 0x8000000
	s_lshl_b32 s95, s83, 23
	s_add_u32 s98, s98, s95
	s_lshl_b32 s95, s93, 20
	s_add_u32 s98, s98, s95
	s_lshl_b32 s95, s94, 10
	s_add_u32 s98, s98, s95
	s_mul_i32 s99, s77, 0x4000000
	s_add_u32 s99, s99, 0x14400000
	s_lshl_b32 s95, s83, 22
	s_add_u32 s99, s99, s95
	s_lshl_b32 s95, s94, 19
	s_add_u32 s99, s99, s95
	s_lshl_b32 s95, s93, 8
	s_add_u32 s99, s99, s95
	v_readlane_b32 s12, v249, 4
	v_readlane_b32 s13, v249, 5
	s_movk_i32 s22, 0x2000
	s_movk_i32 s23, 0x800
	s_mov_b32 s28, 0x40000
	s_branch .Lcv_fin_A1

; #define PW_SYNC do { asm volatile("s_waitcnt lgkmcnt(0)" ::: "memory"); __builtin_amdgcn_s_barrier(); asm volatile("" ::: "memory"); } while (0)
; __device__ __forceinline__ void ph_weights(const Params& p, LAS unsigned char* lds, const int p0, const int p1, const int wi, const int wn) {
;     ...
;     while (hA) {
;         { PW_TOLDS(dA0, a0, a1); PW_SYNC; const TDesc s0 = dA0, s1 = dA1; PW_LOAD(pi + 2 * wn, dA0, dA1, a0, a1, hA); PW_STORE(s0, s1); PW_SYNC; }
;         if (!hB) break;
;         { PW_TOLDS(dB0, b0, b1); PW_SYNC; const TDesc s0 = dB0, s1 = dB1; PW_LOAD(pi + 3 * wn, dB0, dB1, b0, b1, hB); PW_STORE(s0, s1); PW_SYNC; }
;         pi += 2 * wn;
.Lcv_loop:
	s_and_b32 s8, s9, 1
	s_cmp_eq_u32 s8, 0
	s_cbranch_scc1 .Lcv_done
	s_mov_b64 s[84:85], s[14:15]
	s_mov_b32 s69, s23
	s_mov_b32 s75, s28
	s_mov_b32 s87, s29
	s_add_u32 s86, s0, s72
	s_cmp_lt_u32 s86, s71
	s_cbranch_scc1 .Lcv_dec_A
	s_andn2_b32 s9, s9, 1
	s_mov_b32 s22, 0
	s_branch .Lcv_ld_A

; #define PW_SYNC do { asm volatile("s_waitcnt lgkmcnt(0)" ::: "memory"); __builtin_amdgcn_s_barrier(); asm volatile("" ::: "memory"); } while (0)
; __device__ __forceinline__ void ph_weights(const Params& p, LAS unsigned char* lds, const int p0, const int p1, const int wi, const int wn) {
;     ...
;     int pi = p0 + wi; bool hA, hB;
;     PW_LOAD(pi, dA0, dA1, a0, a1, hA);
;     PW_LOAD(pi + wn, dB0, dB1, b0, b1, hB);
;     while (hA) {
;         { PW_TOLDS(dA0, a0, a1); PW_SYNC; const TDesc s0 = dA0, s1 = dA1; PW_LOAD(pi + 2 * wn, dA0, dA1, a0, a1, hA); PW_STORE(s0, s1); PW_SYNC; }
;         if (!hB) break;
;         { PW_TOLDS(dB0, b0, b1); PW_SYNC; const TDesc s0 = dB0, s1 = dB1; PW_LOAD(pi + 3 * wn, dB0, dB1, b0, b1, hB); PW_STORE(s0, s1); PW_SYNC; }
.Lcv_nosc1_At:
	v_cvt_pk_bf16_f32 v18, v18, v22
	v_cvt_pk_bf16_f32 v19, v19, v23
	v_cvt_pk_bf16_f32 v20, v20, v24
	v_cvt_pk_bf16_f32 v21, v21, v25
	v_cvt_pk_bf16_f32 v50, v50, v54
	v_cvt_pk_bf16_f32 v51, v51, v55
	v_cvt_pk_bf16_f32 v52, v52, v56
	v_cvt_pk_bf16_f32 v53, v53, v57
	ds_write_b128 v156, v[18:21] offset:16384
	ds_write_b128 v156, v[50:53] offset:49152
	v_cvt_pk_bf16_f32 v26, v26, v30
	v_cvt_pk_bf16_f32 v27, v27, v31
	v_cvt_pk_bf16_f32 v28, v28, v32
	v_cvt_pk_bf16_f32 v29, v29, v33
	v_cvt_pk_bf16_f32 v58, v58, v62
	v_cvt_pk_bf16_f32 v59, v59, v63
	v_cvt_pk_bf16_f32 v60, v60, v64
	v_cvt_pk_bf16_f32 v61, v61, v65
	ds_write_b128 v157, v[26:29] offset:24576
	ds_write_b128 v157, v[58:61] offset:57344
	v_mad_u32_u24 v177, v168, s22, v169
	s_mov_b64 s[88:89], s[12:13]
	s_add_u32 s90, s12, s22
	s_addc_u32 s91, s13, 0
	s_lshl_b32 s92, s22, 5
	global_load_dwordx2 v[138:139], v170, s[20:21]
	global_load_dwordx2 v[140:141], v170, s[20:21] offset:128
	global_load_dwordx2 v[142:143], v170, s[20:21] offset:256
	global_load_dwordx2 v[144:145], v170, s[20:21] offset:384
	global_load_dwordx4 v[2:5], v177, s[88:89] nt
	global_load_dwordx4 v[34:37], v177, s[88:89] offset:512 nt
	global_load_dwordx4 v[6:9], v177, s[90:91] nt
	global_load_dwordx4 v[38:41], v177, s[90:91] offset:512 nt
	s_add_u32 s88, s88, s92
	s_addc_u32 s89, s89, 0
	s_add_u32 s90, s90, s92
	s_addc_u32 s91, s91, 0
	global_load_dwordx4 v[10:13], v177, s[88:89] nt
	global_load_dwordx4 v[42:45], v177, s[88:89] offset:512 nt
	global_load_dwordx4 v[14:17], v177, s[90:91] nt
	global_load_dwordx4 v[46:49], v177, s[90:91] offset:512 nt
	s_add_u32 s88, s88, s92
	s_addc_u32 s89, s89, 0
	s_add_u32 s90, s90, s92
	s_addc_u32 s91, s91, 0
	global_load_dwordx4 v[18:21], v177, s[88:89] nt
	global_load_dwordx4 v[50:53], v177, s[88:89] offset:512 nt
	global_load_dwordx4 v[22:25], v177, s[90:91] nt
	global_load_dwordx4 v[54:57], v177, s[90:91] offset:512 nt
	s_add_u32 s88, s88, s92
	s_addc_u32 s89, s89, 0
	s_add_u32 s90, s90, s92
	s_addc_u32 s91, s91, 0
	global_load_dwordx4 v[26:29], v177, s[88:89] nt
	global_load_dwordx4 v[58:61], v177, s[88:89] offset:512 nt
	global_load_dwordx4 v[30:33], v177, s[90:91] nt
	global_load_dwordx4 v[62:65], v177, s[90:91] offset:512 nt
	s_waitcnt lgkmcnt(0)
	s_barrier
	v_mad_u32_u24 v178, v175, s69, v176
	s_mov_b64 s[88:89], s[84:85]
	s_add_u32 s90, s84, s75
	s_addc_u32 s91, s85, 0
	s_lshl_b32 s92, s69, 5
	ds_read_b32 v228, v162
	ds_read_b32 v229, v162 offset:512
	ds_read_b32 v230, v162 offset:1024
	ds_read_b32 v231, v162 offset:1536
	ds_read_b32 v232, v162 offset:32768
	ds_read_b32 v233, v162 offset:33280
	ds_read_b32 v234, v162 offset:33792
	ds_read_b32 v235, v162 offset:34304
	s_waitcnt lgkmcnt(0)
	ds_read_b32 v204, v163
	ds_read_b32 v205, v163 offset:512
	ds_read_b32 v206, v163 offset:1024
	ds_read_b32 v207, v163 offset:1536
	ds_read_b32 v208, v163 offset:32768
	ds_read_b32 v209, v163 offset:33280
	ds_read_b32 v210, v163 offset:33792
	ds_read_b32 v211, v163 offset:34304
	global_store_dwordx4 v178, v[228:231], s[88:89] nt
	global_store_dwordx4 v178, v[232:235], s[90:91] nt
	s_add_u32 s88, s88, s92
	s_addc_u32 s89, s89, 0
	s_add_u32 s90, s90, s92
	s_addc_u32 s91, s91, 0
	s_waitcnt lgkmcnt(0)
	ds_read_b32 v228, v164
	ds_read_b32 v229, v164 offset:512
	ds_read_b32 v230, v164 offset:1024
	ds_read_b32 v231, v164 offset:1536
	ds_read_b32 v232, v164 offset:32768
	ds_read_b32 v233, v164 offset:33280
	ds_read_b32 v234, v164 offset:33792
	ds_read_b32 v235, v164 offset:34304
	global_store_dwordx4 v178, v[204:207], s[88:89] nt
	global_store_dwordx4 v178, v[208:211], s[90:91] nt
	s_add_u32 s88, s88, s92
	s_addc_u32 s89, s89, 0
	s_add_u32 s90, s90, s92
	s_addc_u32 s91, s91, 0
	s_waitcnt lgkmcnt(0)
	ds_read_b32 v204, v165
	ds_read_b32 v205, v165 offset:512
	ds_read_b32 v206, v165 offset:1024
	ds_read_b32 v207, v165 offset:1536
	ds_read_b32 v208, v165 offset:32768
	ds_read_b32 v209, v165 offset:33280
	ds_read_b32 v210, v165 offset:33792
	ds_read_b32 v211, v165 offset:34304
	global_store_dwordx4 v178, v[228:231], s[88:89] nt
	global_store_dwordx4 v178, v[232:235], s[90:91] nt
	s_add_u32 s88, s88, s92
	s_addc_u32 s89, s89, 0
	s_add_u32 s90, s90, s92
	s_addc_u32 s91, s91, 0
	s_waitcnt lgkmcnt(0)
	global_store_dwordx4 v178, v[204:207], s[88:89] nt
	global_store_dwordx4 v178, v[208:211], s[90:91] nt
	s_and_b32 s8, s9, 2
	s_cmp_eq_u32 s8, 0
	s_cbranch_scc1 .Lcv_done
	s_mov_b64 s[84:85], s[32:33]
	s_mov_b32 s69, s57
	s_mov_b32 s75, s59
	s_mov_b32 s87, s60
	s_add_u32 s86, s0, s73
	s_cmp_lt_u32 s86, s71
	s_cbranch_scc1 .Lcv_dec_B
	s_andn2_b32 s9, s9, 2
	s_mov_b32 s56, 0
	s_branch .Lcv_ld_B

; #define REP(k) _Pragma("unroll") for (int rep_ = 0; rep_ < 1 + (int)(((REP_MASK) >> (k)) & 1u); ++rep_)
; __global__ void __launch_bounds__(512, 2) mk_fwd(Params p) {
;     ...
;         if (IN(pb + 2)) {
;             if (!split || bx < MIX_GW) {
;                 if (EN(5)) REP(5) ph_fft(p, lds, bx, vG);
;                 __syncthreads();
;                 if (EN(8)) REP(8) ph_mixers(p, l, lds, bx, vG);
;             } else { if (bx - MIX_GW < 4) ph_rbias(p, 0, bx - MIX_GW); ph_weights(p, lds, 240, 6880, bx - MIX_GW, G - MIX_GW); }
.Lcv_done:
	s_waitcnt vmcnt(0)
	s_cmp_eq_u32 s74, 0
	s_cbranch_scc1 .LBB0_902
	v_readlane_b32 s14, v246, 0
	v_readlane_b32 s15, v246, 1
	v_readlane_b32 s20, v246, 2
	v_readlane_b32 s21, v246, 3
	v_readlane_b32 s29, v246, 4
	v_readlane_b32 s30, v246, 5
	v_readlane_b32 s31, v246, 6
	v_readlane_b32 s36, v246, 7
	v_readlane_b32 s37, v246, 8
	v_readlane_b32 s56, v246, 9
	v_readlane_b32 s57, v246, 10
	v_readlane_b32 s69, v246, 11
	s_nop 3
	s_barrier
	s_branch .Lcv_ret986

; #define REP(k) _Pragma("unroll") for (int rep_ = 0; rep_ < 1 + (int)(((REP_MASK) >> (k)) & 1u); ++rep_)
; __global__ void __launch_bounds__(512, 2) mk_fwd(Params p) {
;     ...
;         if (IN(pb + 2)) {
;             if (!split || bx < MIX_GW) {
;                 if (EN(5)) REP(5) ph_fft(p, lds, bx, vG);
;                 __syncthreads();
;                 if (EN(8)) REP(8) ph_mixers(p, l, lds, bx, vG);
;             } else { if (bx - MIX_GW < 4) ph_rbias(p, 0, bx - MIX_GW); ph_weights(p, lds, 240, 6880, bx - MIX_GW, G - MIX_GW); }
.Lcv_hook986:
	v_readlane_b32 s8, v252, 58
	v_readlane_b32 s9, v252, 59
	s_nop 3
	s_and_b64 s[8:9], s[8:9], exec
	s_cbranch_scc0 .Lcv_ret986
	v_readlane_b32 s8, v249, 28
	s_nop 3
	s_cmpk_lt_u32 s8, 0x80
	s_cbranch_scc0 .Lcv_ret986
	s_branch .Lcv_tail

; #define LAS __attribute__((address_space(3)))
; __device__ __forceinline__ void ph_mixers(const Params& p, const int l, LAS unsigned char* lds, const int vbx, const int vG) {
;     ...
;                     const int kp = tl & 63, ta = t0 + 2 * kp;
;                     const float* vs = (const float*)(p.ws + WS_VSS) + (size_t)ta * 8;
;                     const f32x4 sa0 = *(const f32x4*)vs, sa1 = *(const f32x4*)(vs + 4), sb0 = *(const f32x4*)(vs + 8), sb1 = *(const f32x4*)(vs + 12);
;                     u32x4 va[4], vb[4]; f32x4 g0[4], g1[4];
;                     const float* sn = p.in[8] + (size_t)l * 512 + hg * 256 + hw * 128;
; #pragma unroll
;                     for (int i = 0; i < 4; ++i) { const int dc = (tl >> 6) + 4 * i;
;                         const bf16_t* src = PROJ + (size_t)ta * NPROJ + PC_V + hg * 256 + hw * 128 + 8 * dc;
;                         va[i] = *(const u32x4*)src; vb[i] = *(const u32x4*)(src + NPROJ);
;                         g0[i] = *(const f32x4*)(sn + 8 * dc); g1[i] = *(const f32x4*)(sn + 8 * dc + 4); }
;                     const float ra = 1.0f / sqrtf((((sa0[0] + sa0[1]) + (sa0[2] + sa0[3])) + ((sa1[0] + sa1[1]) + (sa1[2] + sa1[3]))) * (1.f / 512.f) + EPS);
;                     const float rb = 1.0f / sqrtf((((sb0[0] + sb0[1]) + (sb0[2] + sb0[3])) + ((sb1[0] + sb1[1]) + (sb1[2] + sb1[3]))) * (1.f / 512.f) + EPS);
; #pragma unroll
;                     for (int i = 0; i < 4; ++i) { const int dc = (tl >> 6) + 4 * i;
;                         LAS unsigned* o = Vt32 + (8 * dc) * (VTSG / 2) + kp;
;                         o[0 * (VTSG / 2)] = pk2(bflo(va[i].x) * ra * g0[i][0], bflo(vb[i].x) * rb * g0[i][0]); o[1 * (VTSG / 2)] = pk2(bfhi(va[i].x) * ra * g0[i][1], bfhi(vb[i].x) * rb * g0[i][1]);
;                         o[2 * (VTSG / 2)] = pk2(bflo(va[i].y) * ra * g0[i][2], bflo(vb[i].y) * rb * g0[i][2]); o[3 * (VTSG / 2)] = pk2(bfhi(va[i].y) * ra * g0[i][3], bfhi(vb[i].y) * rb * g0[i][3]);
;                         o[4 * (VTSG / 2)] = pk2(bflo(va[i].z) * ra * g1[i][0], bflo(vb[i].z) * rb * g1[i][0]); o[5 * (VTSG / 2)] = pk2(bfhi(va[i].z) * ra * g1[i][1], bfhi(vb[i].z) * rb * g1[i][1]);
;                         o[6 * (VTSG / 2)] = pk2(bflo(va[i].w) * ra * g1[i][2], bflo(vb[i].w) * rb * g1[i][2]); o[7 * (VTSG / 2)] = pk2(bfhi(va[i].w) * ra * g1[i][3], bfhi(vb[i].w) * rb * g1[i][3]); }
.LBB0_984:
	s_andn2_saveexec_b64 s[12:13], s[34:35]
	s_cbranch_execz .LBB0_921
	v_and_b32_e32 v74, 63, v34
	v_lshl_or_b32 v4, v74, 1, v4
	v_ashrrev_i32_e32 v5, 31, v4
	v_readlane_b32 s8, v253, 63
	v_lshlrev_b64 v[6:7], 5, v[4:5]
	v_readlane_b32 s9, v254, 0
	v_lshlrev_b32_e32 v194, 10, v3
	v_mov_b64_e32 v[8:9], s[14:15]
	v_lshl_add_u64 v[6:7], s[8:9], 0, v[6:7]
	global_load_dwordx4 v[66:69], v[6:7], off offset:48
	global_load_dwordx4 v[70:73], v[6:7], off offset:32
	global_load_dwordx4 v[78:81], v[6:7], off offset:16
	global_load_dwordx4 v[106:109], v[6:7], off
	v_lshl_add_u64 v[6:7], v[122:123], 0, v[194:195]
	v_mad_i64_i32 v[4:5], s[8:9], v4, s6, v[8:9]
	v_lshlrev_b32_e32 v194, 9, v3
	v_lshl_add_u64 v[2:3], v[4:5], 0, v[194:195]
	v_lshrrev_b32_e32 v4, 3, v34
	v_mov_b32_e32 v125, v195
	v_and_b32_e32 v76, 24, v4
	v_lshl_add_u64 v[2:3], v[2:3], 0, v[124:125]
	v_lshlrev_b32_e32 v194, 1, v76
	v_lshl_add_u64 v[2:3], v[2:3], 0, v[194:195]
	s_movk_i32 s0, 0x1000
	v_add_co_u32_e32 v8, vcc, s0, v2
	global_load_dwordx4 v[46:49], v[2:3], off offset:1024
	s_nop 0
	v_addc_co_u32_e32 v9, vcc, 0, v3, vcc
	global_load_dwordx4 v[50:53], v[8:9], off offset:3584
	v_lshlrev_b32_e32 v194, 2, v76
	v_lshl_add_u64 v[26:27], v[6:7], 0, v[194:195]
	global_load_dwordx4 v[58:61], v[26:27], off offset:16
	global_load_dwordx4 v[62:65], v[26:27], off
	global_load_dwordx4 v[42:45], v[2:3], off offset:1088
	global_load_dwordx4 v[38:41], v[8:9], off offset:3648
	global_load_dwordx4 v[34:37], v[26:27], off offset:144
	global_load_dwordx4 v[54:57], v[26:27], off offset:128
	global_load_dwordx4 v[22:25], v[2:3], off offset:1152
	global_load_dwordx4 v[18:21], v[8:9], off offset:3712
	global_load_dwordx4 v[14:17], v[26:27], off offset:272
	global_load_dwordx4 v[30:33], v[26:27], off offset:256
	s_nop 0
	global_load_dwordx4 v[2:5], v[2:3], off offset:1216
	s_nop 0
	global_load_dwordx4 v[10:13], v[8:9], off offset:3776
	s_nop 0
	global_load_dwordx4 v[6:9], v[26:27], off offset:400
	s_nop 0
	global_load_dwordx4 v[26:29], v[26:27], off offset:384
	s_waitcnt vmcnt(19)
	v_add_f32_e32 v66, v66, v67
	s_waitcnt vmcnt(18)
	v_add_f32_e32 v70, v70, v71
	v_add_f32_e32 v71, v72, v73
	s_waitcnt vmcnt(16)
	v_add_f32_e32 v75, v106, v107
	v_add_f32_e32 v77, v108, v109
	v_add_f32_e32 v75, v75, v77
	v_add_f32_e32 v77, v78, v79
	v_add_f32_e32 v78, v80, v81
	v_add_f32_e32 v77, v77, v78
	v_add_f32_e32 v75, v75, v77
	v_fmamk_f32 v75, v75, 0x3b000000, v217
	v_cmp_gt_f32_e32 vcc, s5, v75
	v_mul_f32_e32 v77, 0x4f800000, v75
	v_add_f32_e32 v67, v68, v69
	v_cndmask_b32_e32 v75, v75, v77, vcc
	v_sqrt_f32_e32 v77, v75
	v_add_f32_e32 v70, v70, v71
	v_add_f32_e32 v66, v66, v67
	v_add_f32_e32 v66, v70, v66
	v_add_u32_e32 v78, -1, v77
	v_fma_f32 v79, -v78, v77, v75
	v_cmp_ge_f32_e64 s[34:35], 0, v79
	v_add_u32_e32 v79, 1, v77
	v_fmamk_f32 v66, v66, 0x3b000000, v217
	v_cndmask_b32_e64 v78, v77, v78, s[34:35]
	v_fma_f32 v77, -v79, v77, v75
	v_cmp_lt_f32_e64 s[34:35], 0, v77
	v_mul_f32_e32 v67, 0x4f800000, v66
	s_nop 0
	v_cndmask_b32_e64 v77, v78, v79, s[34:35]
	v_mul_f32_e32 v78, 0x37800000, v77
	v_cndmask_b32_e32 v77, v77, v78, vcc
	v_cmp_class_f32_e32 vcc, v75, v219
	s_nop 1
	v_cndmask_b32_e32 v75, v77, v75, vcc
	v_div_scale_f32 v77, s[8:9], v75, v75, 1.0
	v_rcp_f32_e32 v78, v77
	s_nop 0
	v_fma_f32 v79, -v77, v78, 1.0
	v_fmac_f32_e32 v78, v79, v78
	v_div_scale_f32 v79, vcc, 1.0, v75, 1.0
	v_mul_f32_e32 v80, v79, v78
	v_fma_f32 v81, -v77, v80, v79
	v_fmac_f32_e32 v80, v81, v78
	v_fma_f32 v77, -v77, v80, v79
	v_div_fmas_f32 v77, v77, v78, v80
	v_cmp_gt_f32_e32 vcc, s5, v66
	v_div_fixup_f32 v75, v77, v75, 1.0
	s_nop 0
	v_cndmask_b32_e32 v66, v66, v67, vcc
	v_sqrt_f32_e32 v67, v66
	s_nop 0
	v_add_u32_e32 v68, -1, v67
	v_fma_f32 v69, -v68, v67, v66
	v_cmp_ge_f32_e64 s[34:35], 0, v69
	v_add_u32_e32 v69, 1, v67
	s_nop 0
	v_cndmask_b32_e64 v68, v67, v68, s[34:35]
	v_fma_f32 v67, -v69, v67, v66
	v_cmp_lt_f32_e64 s[34:35], 0, v67
	s_nop 1
	v_cndmask_b32_e64 v67, v68, v69, s[34:35]
	v_mul_f32_e32 v68, 0x37800000, v67
	v_cndmask_b32_e32 v67, v67, v68, vcc
	v_cmp_class_f32_e32 vcc, v66, v219
	s_nop 1
	v_cndmask_b32_e32 v66, v67, v66, vcc
	v_div_scale_f32 v67, s[8:9], v66, v66, 1.0
	v_rcp_f32_e32 v68, v67
	s_nop 0
	v_fma_f32 v69, -v67, v68, 1.0
	v_fmac_f32_e32 v68, v69, v68
	v_div_scale_f32 v69, vcc, 1.0, v66, 1.0
	v_mul_f32_e32 v70, v69, v68
	v_fma_f32 v71, -v67, v70, v69
	v_fmac_f32_e32 v70, v71, v68
	v_fma_f32 v67, -v67, v70, v69
	v_div_fmas_f32 v67, v67, v68, v70
	v_div_fixup_f32 v66, v67, v66, 1.0
	v_lshlrev_b32_e32 v67, 2, v74
	v_mul_u32_u24_e32 v68, 0x110, v76
	v_add3_u32 v67, v167, v67, v68
	s_waitcnt vmcnt(15)
	v_lshlrev_b32_e32 v68, 16, v46
	v_and_b32_e32 v46, 0xffff0000, v46
	s_waitcnt vmcnt(14)
	v_lshlrev_b32_e32 v69, 16, v50
	v_mul_f32_e32 v46, v75, v46
	v_and_b32_e32 v50, 0xffff0000, v50
	v_mul_f32_e32 v68, v75, v68
	v_mul_f32_e32 v69, v66, v69
	s_waitcnt vmcnt(12)
; #define LAS __attribute__((address_space(3)))
; __device__ __forceinline__ unsigned pk2(float lo, float hi) { unsigned r; asm("v_cvt_pk_bf16_f32 %0, %1, %2" : "=v"(r) : "v"(lo), "v"(hi)); return r; }
; __device__ __forceinline__ float bflo(unsigned u) { return __uint_as_float(u << 16); }
; __device__ __forceinline__ float bfhi(unsigned u) { return __uint_as_float(u & 0xffff0000u); }
; __device__ __forceinline__ void ph_mixers(const Params& p, const int l, LAS unsigned char* lds, const int vbx, const int vG) {
;     ...
; #pragma unroll
;                     for (int i = 0; i < 4; ++i) { const int dc = (tl >> 6) + 4 * i;
;                         LAS unsigned* o = Vt32 + (8 * dc) * (VTSG / 2) + kp;
;                         o[0 * (VTSG / 2)] = pk2(bflo(va[i].x) * ra * g0[i][0], bflo(vb[i].x) * rb * g0[i][0]); o[1 * (VTSG / 2)] = pk2(bfhi(va[i].x) * ra * g0[i][1], bfhi(vb[i].x) * rb * g0[i][1]);
;                         o[2 * (VTSG / 2)] = pk2(bflo(va[i].y) * ra * g0[i][2], bflo(vb[i].y) * rb * g0[i][2]); o[3 * (VTSG / 2)] = pk2(bfhi(va[i].y) * ra * g0[i][3], bfhi(vb[i].y) * rb * g0[i][3]);
;                         o[4 * (VTSG / 2)] = pk2(bflo(va[i].z) * ra * g1[i][0], bflo(vb[i].z) * rb * g1[i][0]); o[5 * (VTSG / 2)] = pk2(bfhi(va[i].z) * ra * g1[i][1], bfhi(vb[i].z) * rb * g1[i][1]);
;                         o[6 * (VTSG / 2)] = pk2(bflo(va[i].w) * ra * g1[i][2], bflo(vb[i].w) * rb * g1[i][2]); o[7 * (VTSG / 2)] = pk2(bfhi(va[i].w) * ra * g1[i][3], bfhi(vb[i].w) * rb * g1[i][3]); }
	v_mul_f32_e32 v46, v63, v46
	v_mul_f32_e32 v50, v66, v50
	v_mul_f32_e32 v68, v62, v68
	v_mul_f32_e32 v62, v62, v69
	v_mul_f32_e32 v50, v63, v50
	v_cvt_pk_bf16_f32 v46, v46, v50
	v_cvt_pk_bf16_f32 v62, v68, v62
	ds_write2_b32 v67, v62, v46 offset1:68
	v_lshlrev_b32_e32 v46, 16, v47
	v_lshlrev_b32_e32 v50, 16, v51
	v_mul_f32_e32 v46, v75, v46
	v_mul_f32_e32 v50, v66, v50
	v_mul_f32_e32 v46, v64, v46
	v_mul_f32_e32 v50, v64, v50
	v_and_b32_e32 v47, 0xffff0000, v47
	v_cvt_pk_bf16_f32 v46, v46, v50
	v_mul_f32_e32 v47, v75, v47
	v_and_b32_e32 v50, 0xffff0000, v51
	v_mul_f32_e32 v47, v65, v47
	v_mul_f32_e32 v50, v66, v50
	v_mul_f32_e32 v50, v65, v50
	v_cvt_pk_bf16_f32 v47, v47, v50
	ds_write2_b32 v67, v46, v47 offset0:136 offset1:204
	v_lshlrev_b32_e32 v46, 16, v48
	v_lshlrev_b32_e32 v47, 16, v52
	v_mul_f32_e32 v46, v75, v46
	v_mul_f32_e32 v47, v66, v47
	v_mul_f32_e32 v46, v58, v46
	v_mul_f32_e32 v47, v58, v47
	v_cvt_pk_bf16_f32 v46, v46, v47
	v_and_b32_e32 v47, 0xffff0000, v48
	v_and_b32_e32 v48, 0xffff0000, v52
	v_mul_f32_e32 v47, v75, v47
	v_mul_f32_e32 v48, v66, v48
	v_mul_f32_e32 v47, v59, v47
	v_mul_f32_e32 v48, v59, v48
	v_cvt_pk_bf16_f32 v47, v47, v48
	v_add_u32_e32 v48, 0x400, v67
	ds_write2_b32 v48, v46, v47 offset0:16 offset1:84
	v_lshlrev_b32_e32 v46, 16, v49
	v_lshlrev_b32_e32 v47, 16, v53
	v_mul_f32_e32 v46, v75, v46
	v_mul_f32_e32 v47, v66, v47
	v_mul_f32_e32 v46, v60, v46
	v_mul_f32_e32 v47, v60, v47
	v_cvt_pk_bf16_f32 v46, v46, v47
	v_and_b32_e32 v47, 0xffff0000, v49
	v_mul_f32_e32 v47, v75, v47
	v_and_b32_e32 v49, 0xffff0000, v53
	v_mul_f32_e32 v47, v61, v47
	v_mul_f32_e32 v49, v66, v49
	v_mul_f32_e32 v49, v61, v49
	v_cvt_pk_bf16_f32 v47, v47, v49
	ds_write2_b32 v48, v46, v47 offset0:152 offset1:220
	s_waitcnt vmcnt(11)
	v_lshlrev_b32_e32 v46, 16, v42
	s_waitcnt vmcnt(10)
	v_lshlrev_b32_e32 v47, 16, v38
	v_and_b32_e32 v42, 0xffff0000, v42
	v_and_b32_e32 v38, 0xffff0000, v38
	v_mul_f32_e32 v42, v75, v42
	v_mul_f32_e32 v38, v66, v38
	v_mul_f32_e32 v46, v75, v46
	s_waitcnt vmcnt(8)
	v_mul_f32_e32 v42, v55, v42
	v_mul_f32_e32 v38, v55, v38
	v_mul_f32_e32 v46, v54, v46
	v_mul_f32_e32 v47, v66, v47
	v_cvt_pk_bf16_f32 v38, v42, v38
	v_add_u32_e32 v42, 0x2000, v67
	v_mul_f32_e32 v47, v54, v47
	v_cvt_pk_bf16_f32 v46, v46, v47
	ds_write2_b32 v42, v46, v38 offset0:128 offset1:196
	v_lshlrev_b32_e32 v38, 16, v43
	v_lshlrev_b32_e32 v42, 16, v39
	v_mul_f32_e32 v38, v75, v38
	v_mul_f32_e32 v42, v66, v42
	v_mul_f32_e32 v38, v56, v38
	v_mul_f32_e32 v42, v56, v42
	v_cvt_pk_bf16_f32 v38, v38, v42
	v_and_b32_e32 v42, 0xffff0000, v43
	v_and_b32_e32 v39, 0xffff0000, v39
	v_mul_f32_e32 v42, v75, v42
	v_mul_f32_e32 v39, v66, v39
	v_mul_f32_e32 v42, v57, v42
	v_mul_f32_e32 v39, v57, v39
	v_cvt_pk_bf16_f32 v39, v42, v39
	v_add_u32_e32 v42, 0x2400, v67
	ds_write2_b32 v42, v38, v39 offset0:8 offset1:76
	v_lshlrev_b32_e32 v38, 16, v44
	v_lshlrev_b32_e32 v39, 16, v40
	v_mul_f32_e32 v38, v75, v38
	v_mul_f32_e32 v39, v66, v39
	v_mul_f32_e32 v38, v38, v34
	v_mul_f32_e32 v34, v34, v39
	v_cvt_pk_bf16_f32 v34, v38, v34
	v_and_b32_e32 v38, 0xffff0000, v44
	v_and_b32_e32 v39, 0xffff0000, v40
	v_mul_f32_e32 v38, v75, v38
	v_mul_f32_e32 v39, v66, v39
	v_mul_f32_e32 v38, v38, v35
	v_mul_f32_e32 v35, v35, v39
	v_cvt_pk_bf16_f32 v35, v38, v35
	ds_write2_b32 v42, v34, v35 offset0:144 offset1:212
	v_lshlrev_b32_e32 v34, 16, v45
	v_lshlrev_b32_e32 v35, 16, v41
	v_mul_f32_e32 v34, v75, v34
	v_mul_f32_e32 v35, v66, v35
	v_mul_f32_e32 v34, v34, v36
	v_mul_f32_e32 v35, v36, v35
	v_cvt_pk_bf16_f32 v34, v34, v35
	v_and_b32_e32 v35, 0xffff0000, v45
	v_and_b32_e32 v36, 0xffff0000, v41
	v_mul_f32_e32 v35, v75, v35
	v_mul_f32_e32 v36, v66, v36
	v_mul_f32_e32 v35, v35, v37
	v_mul_f32_e32 v36, v37, v36
	v_cvt_pk_bf16_f32 v35, v35, v36
	v_add_u32_e32 v36, 0x2800, v67
	ds_write2_b32 v36, v34, v35 offset0:24 offset1:92
	s_waitcnt vmcnt(7)
	v_lshlrev_b32_e32 v34, 16, v22
	s_waitcnt vmcnt(6)
	v_lshlrev_b32_e32 v35, 16, v18
	v_and_b32_e32 v22, 0xffff0000, v22
	v_and_b32_e32 v18, 0xffff0000, v18
	v_mul_f32_e32 v34, v75, v34
	v_mul_f32_e32 v35, v66, v35
	v_mul_f32_e32 v22, v75, v22
	v_mul_f32_e32 v18, v66, v18
	s_waitcnt vmcnt(4)
; #define LAS __attribute__((address_space(3)))
; __device__ __forceinline__ unsigned pk2(float lo, float hi) { unsigned r; asm("v_cvt_pk_bf16_f32 %0, %1, %2" : "=v"(r) : "v"(lo), "v"(hi)); return r; }
; __device__ __forceinline__ float bflo(unsigned u) { return __uint_as_float(u << 16); }
; __device__ __forceinline__ float bfhi(unsigned u) { return __uint_as_float(u & 0xffff0000u); }
; __device__ __forceinline__ void ph_mixers(const Params& p, const int l, LAS unsigned char* lds, const int vbx, const int vG) {
;     ...
; #pragma unroll
;                     for (int i = 0; i < 4; ++i) { const int dc = (tl >> 6) + 4 * i;
;                         LAS unsigned* o = Vt32 + (8 * dc) * (VTSG / 2) + kp;
;                         o[0 * (VTSG / 2)] = pk2(bflo(va[i].x) * ra * g0[i][0], bflo(vb[i].x) * rb * g0[i][0]); o[1 * (VTSG / 2)] = pk2(bfhi(va[i].x) * ra * g0[i][1], bfhi(vb[i].x) * rb * g0[i][1]);
;                         o[2 * (VTSG / 2)] = pk2(bflo(va[i].y) * ra * g0[i][2], bflo(vb[i].y) * rb * g0[i][2]); o[3 * (VTSG / 2)] = pk2(bfhi(va[i].y) * ra * g0[i][3], bfhi(vb[i].y) * rb * g0[i][3]);
;                         o[4 * (VTSG / 2)] = pk2(bflo(va[i].z) * ra * g1[i][0], bflo(vb[i].z) * rb * g1[i][0]); o[5 * (VTSG / 2)] = pk2(bfhi(va[i].z) * ra * g1[i][1], bfhi(vb[i].z) * rb * g1[i][1]);
;                         o[6 * (VTSG / 2)] = pk2(bflo(va[i].w) * ra * g1[i][2], bflo(vb[i].w) * rb * g1[i][2]); o[7 * (VTSG / 2)] = pk2(bfhi(va[i].w) * ra * g1[i][3], bfhi(vb[i].w) * rb * g1[i][3]); }
;     ...
;         __syncthreads();
;     }
	v_mul_f32_e32 v34, v30, v34
	v_mul_f32_e32 v30, v30, v35
	v_mul_f32_e32 v22, v31, v22
	v_mul_f32_e32 v18, v31, v18
	v_cvt_pk_bf16_f32 v30, v34, v30
	v_cvt_pk_bf16_f32 v18, v22, v18
	v_add_u32_e32 v22, 0x4400, v67
	ds_write2_b32 v22, v30, v18 offset1:68
	v_lshlrev_b32_e32 v18, 16, v23
	v_lshlrev_b32_e32 v30, 16, v19
	v_and_b32_e32 v19, 0xffff0000, v19
	v_mul_f32_e32 v18, v75, v18
	v_and_b32_e32 v23, 0xffff0000, v23
	v_mul_f32_e32 v19, v66, v19
	v_mul_f32_e32 v18, v32, v18
	v_mul_f32_e32 v30, v66, v30
	v_mul_f32_e32 v23, v75, v23
	v_mul_f32_e32 v19, v33, v19
	v_mul_f32_e32 v30, v32, v30
	v_cvt_pk_bf16_f32 v18, v18, v30
	v_mul_f32_e32 v23, v33, v23
	v_cvt_pk_bf16_f32 v19, v23, v19
	ds_write2_b32 v22, v18, v19 offset0:136 offset1:204
	v_lshlrev_b32_e32 v18, 16, v24
	v_lshlrev_b32_e32 v19, 16, v20
	v_mul_f32_e32 v18, v75, v18
	v_mul_f32_e32 v19, v66, v19
	v_mul_f32_e32 v18, v18, v14
	v_mul_f32_e32 v14, v14, v19
	v_cvt_pk_bf16_f32 v14, v18, v14
	v_and_b32_e32 v18, 0xffff0000, v24
	v_and_b32_e32 v19, 0xffff0000, v20
	v_mul_f32_e32 v18, v75, v18
	v_mul_f32_e32 v19, v66, v19
	v_mul_f32_e32 v18, v18, v15
	v_mul_f32_e32 v15, v15, v19
	v_cvt_pk_bf16_f32 v15, v18, v15
	v_add_u32_e32 v18, 0x4800, v67
	ds_write2_b32 v18, v14, v15 offset0:16 offset1:84
	v_lshlrev_b32_e32 v14, 16, v25
	v_lshlrev_b32_e32 v15, 16, v21
	v_mul_f32_e32 v14, v75, v14
	v_mul_f32_e32 v15, v66, v15
	v_mul_f32_e32 v14, v14, v16
	v_mul_f32_e32 v15, v16, v15
	v_cvt_pk_bf16_f32 v14, v14, v15
	v_and_b32_e32 v15, 0xffff0000, v25
	v_mul_f32_e32 v15, v75, v15
	v_and_b32_e32 v16, 0xffff0000, v21
	v_mul_f32_e32 v15, v15, v17
	v_mul_f32_e32 v16, v66, v16
	v_mul_f32_e32 v16, v17, v16
	v_cvt_pk_bf16_f32 v15, v15, v16
	ds_write2_b32 v18, v14, v15 offset0:152 offset1:220
	s_waitcnt vmcnt(3)
	v_lshlrev_b32_e32 v14, 16, v2
	s_waitcnt vmcnt(2)
	v_lshlrev_b32_e32 v15, 16, v10
	v_and_b32_e32 v2, 0xffff0000, v2
	v_and_b32_e32 v10, 0xffff0000, v10
	v_mul_f32_e32 v2, v75, v2
	v_mul_f32_e32 v10, v66, v10
	v_mul_f32_e32 v14, v75, v14
	s_waitcnt vmcnt(0)
	v_mul_f32_e32 v2, v27, v2
	v_mul_f32_e32 v10, v27, v10
	v_mul_f32_e32 v14, v26, v14
	v_mul_f32_e32 v15, v66, v15
	v_cvt_pk_bf16_f32 v2, v2, v10
	v_add_u32_e32 v10, 0x6400, v67
	v_mul_f32_e32 v15, v26, v15
	v_cvt_pk_bf16_f32 v14, v14, v15
	ds_write2_b32 v10, v14, v2 offset0:128 offset1:196
	v_lshlrev_b32_e32 v2, 16, v3
	v_lshlrev_b32_e32 v10, 16, v11
	v_mul_f32_e32 v2, v75, v2
	v_mul_f32_e32 v10, v66, v10
	v_mul_f32_e32 v2, v28, v2
	v_mul_f32_e32 v10, v28, v10
	v_cvt_pk_bf16_f32 v2, v2, v10
	v_and_b32_e32 v3, 0xffff0000, v3
	v_and_b32_e32 v10, 0xffff0000, v11
	v_mul_f32_e32 v3, v75, v3
	v_mul_f32_e32 v10, v66, v10
	v_mul_f32_e32 v3, v29, v3
	v_mul_f32_e32 v10, v29, v10
	v_cvt_pk_bf16_f32 v3, v3, v10
	v_add_u32_e32 v10, 0x6800, v67
	ds_write2_b32 v10, v2, v3 offset0:8 offset1:76
	v_lshlrev_b32_e32 v2, 16, v4
	v_lshlrev_b32_e32 v3, 16, v12
	v_mul_f32_e32 v2, v75, v2
	v_mul_f32_e32 v3, v66, v3
	v_mul_f32_e32 v2, v2, v6
	v_mul_f32_e32 v3, v6, v3
	v_cvt_pk_bf16_f32 v2, v2, v3
	v_and_b32_e32 v3, 0xffff0000, v4
	v_mul_f32_e32 v3, v75, v3
	v_and_b32_e32 v4, 0xffff0000, v12
	v_mul_f32_e32 v3, v3, v7
	v_mul_f32_e32 v4, v66, v4
	v_mul_f32_e32 v4, v7, v4
	v_cvt_pk_bf16_f32 v3, v3, v4
	ds_write2_b32 v10, v2, v3 offset0:144 offset1:212
	v_lshlrev_b32_e32 v2, 16, v5
	v_lshlrev_b32_e32 v3, 16, v13
	v_mul_f32_e32 v2, v75, v2
	v_mul_f32_e32 v3, v66, v3
	v_mul_f32_e32 v2, v2, v8
	v_mul_f32_e32 v3, v8, v3
	v_cvt_pk_bf16_f32 v2, v2, v3
	v_and_b32_e32 v3, 0xffff0000, v5
	v_and_b32_e32 v4, 0xffff0000, v13
	v_mul_f32_e32 v3, v75, v3
	v_mul_f32_e32 v4, v66, v4
	v_mul_f32_e32 v3, v3, v9
	v_mul_f32_e32 v4, v9, v4
	v_cvt_pk_bf16_f32 v3, v3, v4
	v_add_u32_e32 v4, 0x6c00, v67
	ds_write2_b32 v4, v2, v3 offset0:24 offset1:92
	s_branch .LBB0_921
.LBB0_986:
	s_branch .Lcv_hook986
.Lcv_ret986:
	v_readlane_b32 s0, v249, 52
	v_readlane_b32 s8, v249, 8
	s_add_i32 s4, s0, 4
	v_readlane_b32 s9, v249, 9
	s_cmp_ge_i32 s4, s9
	s_cbranch_scc1 .LBB0_1034
	s_waitcnt vmcnt(0)
	s_waitcnt vmcnt(0) lgkmcnt(0)
	s_barrier
	s_mov_b64 s[12:13], exec
	v_readlane_b32 s8, v252, 33
	v_readlane_b32 s9, v252, 34
	s_and_b64 s[8:9], s[12:13], s[8:9]
	s_mov_b64 exec, s[8:9]
	s_cbranch_execz .LBB0_1033
	v_readlane_b32 s0, v252, 56
	s_waitcnt vmcnt(0) expcnt(0) lgkmcnt(0)
	s_nop 0
	v_mov_b32_e32 v1, s0
	ds_read_b32 v3, v1
	v_readlane_b32 s0, v252, 57
	s_waitcnt lgkmcnt(0)
	v_cmp_ne_u32_e32 vcc, 0, v3
	v_mov_b32_e32 v1, s0
	ds_read_b32 v2, v1
	s_cbranch_vccnz .LBB0_1003
	s_mov_b32 s8, 1
	s_branch .LBB0_991
